# BEST + dedicated conversion pass striped by quarter-XCD groups (at most 8 streaming CUs per XCD per slot)
# baseline (speedup 1.0000x reference)
; __device__ __forceinline__ unsigned xb_ld(unsigned* p)              { return __hip_atomic_load(p, __ATOMIC_RELAXED, __HIP_MEMORY_SCOPE_AGENT); }
; #define XB_SPIN(cond, bar) do { unsigned _sp = 0; while (cond) { __builtin_amdgcn_s_sleep(1); \
;     if ((++_sp & 255u) == 0u) { if (xb_ld(&(bar)[XB_TMO])) break; if (_sp > XB_SPIN_CAP) { atomicAdd(&(bar)[XB_TMO], 1u); break; } } } } while (0)
;     ...
;     int R0, C0, R1, C1; stage_rc(tid * 16, R0, C0); stage_rc(tid * 16 + 8192, R1, C1);
;     unsigned voffB[2];
;     { const int Rb0 = Epi::PERM ? ((R0 & ~31) + perm32(R0 & 31)) : R0, Rb1 = Epi::PERM ? ((R1 & ~31) + perm32(R1 & 31)) : R1;
;       voffB[0] = (unsigned)(Rb0 * 64 + C0) * 2u; voffB[1] = (unsigned)(Rb1 * 64 + C1) * 2u; }
;     const unsigned kstep = (unsigned)(BK * 2);
;     const unsigned kstepB = 256u * 64u * 2u;
;     const unsigned hstepB = (unsigned)HALF * 64u * 2u;
;     const unsigned ldsw = (unsigned)wid * 1024u;
;     const int aoff = lds_byte(wr * 64 + fr, fq * 8), boff = lds_byte(wc * 32 + fr, fq * 8);
; __global__ void __launch_bounds__(NTHREADS, 2) hymba_fwd(Params P) {
;     ...
;         const int nu = (S.nwg - blk + G - 1) / G;
;         if (tid == 0) { unsigned* bw = (unsigned*)(P.ws + WS_BAR);
;             XB_SPIN(xb_ld(wincnt) < (unsigned)G, bw);
;             int lastpm = -1;
;             for (int k = 0; k < nu; ++k) { g8::Unit uk; if (!S.next(k, uk)) break; if (uk.pm != lastpm) { lastpm = uk.pm; XB_SPIN(xb_ld(hcnt + uk.pm) < 4u, bw); } }
;             __builtin_amdgcn_fence(__ATOMIC_ACQUIRE, "agent"); asm volatile("s_waitcnt vmcnt(0)" ::: "memory"); }
;         __syncthreads();
;         NIN = (nu * (DM / 128) - 2) >> 2; NIN = NIN < 0 ? 0 : (NIN > nU ? nU : NIN);
;         int slot = ((blk & 7) + 3 * (((blk >> 3) & 7) >> 2)) % 6; slot = slot < nu ? slot : nu;
.LBB0_218:
	s_or_b64 exec, exec, s[0:1]
	s_ashr_i32 s0, s30, 31
	v_readlane_b32 s36, v254, 39
	v_readlane_b32 s37, v254, 40
	s_add_u32 s10, s36, 0x1f41e000
	s_addc_u32 s11, s37, 0
	s_add_u32 s12, s36, 0x2d41e000
	s_mul_i32 s1, s29, s8
	s_addc_u32 s13, s37, 0
	s_sub_i32 s1, s27, s1
	s_xor_b32 s0, s0, s28
	s_add_i32 s3, s29, 1
	s_sub_i32 s4, s1, s8
	s_cmp_ge_u32 s1, s8
	s_cselect_b32 s3, s3, s29
	s_cselect_b32 s1, s4, s1
	s_add_i32 s4, s3, 1
	s_cmp_ge_u32 s1, s8
	s_cselect_b32 s1, s4, s3
	s_xor_b32 s1, s1, s0
	s_sub_i32 s3, s1, s0
	s_lshl_b32 s0, s9, 4
	s_add_i32 s0, s0, -2
	s_ashr_i32 s0, s0, 2
	s_min_i32 s1, s0, s3
	s_cmp_gt_i32 s0, -1
	s_cselect_b32 s5, s1, 0
	s_bfe_u32 s1, s2, 0x10004
	s_and_b32 s0, s2, 7
	s_mul_i32 s1, s1, 3
	s_add_i32 s4, s1, s0
	s_bfe_u32 s1, s2, 0x10005
	s_add_i32 s4, s4, s1
	v_sub_co_u32_e64 v1, s[0:1], s4, 6
	s_and_b64 s[0:1], s[0:1], exec
	v_readfirstlane_b32 s0, v1
	v_lshlrev_b32_e32 v1, 4, v0
	s_waitcnt vmcnt(7)
	v_and_b32_e32 v2, 32, v0
	s_cselect_b32 s0, s4, s0
	v_bitop3_b32 v1, v1, v2, 48 bitop3:0x6c
	s_min_i32 s62, s0, s9
	s_lshl_b32 s1, s3, 2
	v_and_or_b32 v2, v0, 64, v1
	v_bfe_u32 v1, v0, 3, 25
	v_lshrrev_b32_e32 v3, 3, v0
	v_bfe_u32 v4, v0, 2, 4
	s_waitcnt vmcnt(4)
	v_or_b32_e32 v6, 64, v1
	s_movk_i32 s0, 0x70
	s_add_u32 s6, s36, 0x4e6000
	v_and_or_b32 v5, v3, 48, v4
	v_and_or_b32 v4, v6, s0, v4
	v_lshrrev_b32_e32 v6, 1, v0
	v_lshrrev_b32_e32 v7, 5, v0
	v_bfe_u32 v8, v0, 2, 2
	s_movk_i32 s0, 0x60
	s_addc_u32 s7, s37, 0
	v_readlane_b32 s38, v254, 41
	v_readlane_b32 s39, v254, 42
	v_and_b32_e32 v3, 32, v3
	v_and_b32_e32 v6, 24, v6
	v_and_or_b32 v7, v7, 4, v8
	v_bitop3_b32 v1, v1, s0, 64 bitop3:0xc8
	v_writelane_b32 v254, s6, 50
	s_ashr_i32 s51, s2, 31
	s_add_i32 s52, s1, -1
	v_or3_b32 v3, v3, v7, v6
	v_or3_b32 v6, v6, v1, v7
	v_writelane_b32 v254, s7, 51
	s_add_u32 s53, s36, 0x1341e000
	v_lshl_or_b32 v1, v3, 7, v2
	v_lshl_or_b32 v198, v6, 7, v2
	v_and_b32_e32 v3, 48, v0
	v_lshlrev_b32_e32 v6, 6, v0
	s_movk_i32 s0, 0x3c0
	v_writelane_b32 v254, s1, 52
	s_addc_u32 s54, s37, 0
	s_add_u32 s55, s36, 0x341e000
	v_writelane_b32 v254, s5, 49
	v_and_or_b32 v205, v6, s0, v3
	s_mov_b32 s0, 0
	s_addc_u32 s56, s37, 0
	s_add_i32 s1, s5, 2
	v_writelane_b32 v254, s0, 45
	s_lshl_b32 s64, s33, 1
	s_mul_i32 s58, s33, s1
	v_writelane_b32 v254, s62, 53
	s_lshl_b32 s67, s58, 3
	v_writelane_b32 v254, s64, 55
	s_lshl_b32 s76, s33, 4
	s_add_i32 s1, s5, 3
	v_writelane_b32 v254, s67, 57
	s_lshl_b32 s77, s58, 7
	s_mul_i32 s65, s33, s1
	v_writelane_b32 v254, s76, 58
	v_lshlrev_b32_e32 v8, 2, v0
	s_lshl_b32 s78, s33, 8
	s_lshl_b32 s81, s65, 3
	v_writelane_b32 v254, s77, 59
	v_and_b32_e32 v7, 0x3c0, v6
	v_and_b32_e32 v199, 32, v8
	s_lshl_b32 s79, s58, 4
	s_lshl_b32 s82, s65, 7
	v_writelane_b32 v254, s78, 60
	v_writelane_b32 v255, s81, 0
	v_bitop3_b32 v200, v7, v199, v3 bitop3:0x36
	v_or_b32_e32 v7, 0x80000, v2
	v_lshlrev_b32_e32 v5, 12, v5
	v_lshlrev_b32_e32 v4, 12, v4
	s_lshl_b32 s80, s33, 5
	s_lshl_b32 s83, s65, 4
	v_writelane_b32 v254, s79, 61
	v_writelane_b32 v255, s82, 1
	s_mov_b32 s15, 0
	v_or_b32_e32 v201, v5, v2
	v_or_b32_e32 v202, v4, v2
	v_or_b32_e32 v203, v5, v7
	v_or_b32_e32 v204, v4, v7
	s_mov_b64 s[24:25], -1
	v_mov_b32_e32 v195, 0
	s_mov_b64 s[26:27], 0x80
	s_mov_b32 s70, 0xc2fc0000
	s_movk_i32 s71, 0x2800
	v_mov_b64_e32 v[196:197], 0x4ff
	v_mov_b32_e32 v206, 0x42800000
	v_mov_b32_e32 v207, 0x42000000
	v_not_b32_e32 v208, 63
	v_writelane_b32 v254, s80, 62
	v_writelane_b32 v255, s83, 2
	s_barrier
	s_branch .LBB0_221
